# MoE down-projection output kept in slot order (dense row stores instead of the token-major scatter); the two combining norm phases gather each token's two rows through a per-layer tile-start table
# baseline (speedup 1.0000x reference)
.LBB0_171:
	s_andn2_b64 vcc, exec, s[0:1]
	s_cbranch_vccnz .LBB0_273
	v_readlane_b32 s7, v244, 22
	s_cmp_lg_u32 s7, 0
	s_cbranch_scc0 .LBB0_184
	s_waitcnt vmcnt(9)
	v_and_b32_e32 v247, 63, v0
	v_min_u32_e32 v247, 15, v247
	v_lshlrev_b32_e32 v247, 8, v247
	v_readlane_b32 s100, v244, 22
	s_nop 0
	s_add_i32 s100, s100, -1
	s_lshl_b32 s100, s100, 12
	s_add_i32 s100, s100, 0x4000
	v_add_u32_e32 v247, s100, v247
	v_readlane_b32 s100, v244, 55
	v_readlane_b32 s101, v244, 56
	s_nop 4
	global_load_dword v248, v247, s[100:101] sc1
	s_waitcnt vmcnt(0)
	v_add_u32_e32 v248, 0xff, v248
	v_lshrrev_b32_e32 v248, 8, v248
	s_mov_b32 vcc_lo, 0
	v_readlane_b32 vcc_hi, v248, 0
	s_lshl_b32 s100, vcc_lo, 18
	v_writelane_b32 v255, s100, 0
	s_add_i32 vcc_lo, vcc_lo, vcc_hi
	v_readlane_b32 vcc_hi, v248, 1
	s_lshl_b32 s100, vcc_lo, 18
	v_writelane_b32 v255, s100, 1
	s_add_i32 vcc_lo, vcc_lo, vcc_hi
	v_readlane_b32 vcc_hi, v248, 2
	s_lshl_b32 s100, vcc_lo, 18
	v_writelane_b32 v255, s100, 2
	s_add_i32 vcc_lo, vcc_lo, vcc_hi
	v_readlane_b32 vcc_hi, v248, 3
	s_lshl_b32 s100, vcc_lo, 18
	v_writelane_b32 v255, s100, 3
	s_add_i32 vcc_lo, vcc_lo, vcc_hi
	v_readlane_b32 vcc_hi, v248, 4
	s_lshl_b32 s100, vcc_lo, 18
	v_writelane_b32 v255, s100, 4
	s_add_i32 vcc_lo, vcc_lo, vcc_hi
	v_readlane_b32 vcc_hi, v248, 5
	s_lshl_b32 s100, vcc_lo, 18
	v_writelane_b32 v255, s100, 5
	s_add_i32 vcc_lo, vcc_lo, vcc_hi
	v_readlane_b32 vcc_hi, v248, 6
	s_lshl_b32 s100, vcc_lo, 18
	v_writelane_b32 v255, s100, 6
	s_add_i32 vcc_lo, vcc_lo, vcc_hi
	v_readlane_b32 vcc_hi, v248, 7
	s_lshl_b32 s100, vcc_lo, 18
	v_writelane_b32 v255, s100, 7
	s_add_i32 vcc_lo, vcc_lo, vcc_hi
	v_readlane_b32 vcc_hi, v248, 8
	s_lshl_b32 s100, vcc_lo, 18
	v_writelane_b32 v255, s100, 8
	s_add_i32 vcc_lo, vcc_lo, vcc_hi
	v_readlane_b32 vcc_hi, v248, 9
	s_lshl_b32 s100, vcc_lo, 18
	v_writelane_b32 v255, s100, 9
	s_add_i32 vcc_lo, vcc_lo, vcc_hi
	v_readlane_b32 vcc_hi, v248, 10
	s_lshl_b32 s100, vcc_lo, 18
	v_writelane_b32 v255, s100, 10
	s_add_i32 vcc_lo, vcc_lo, vcc_hi
	v_readlane_b32 vcc_hi, v248, 11
	s_lshl_b32 s100, vcc_lo, 18
	v_writelane_b32 v255, s100, 11
	s_add_i32 vcc_lo, vcc_lo, vcc_hi
	v_readlane_b32 vcc_hi, v248, 12
	s_lshl_b32 s100, vcc_lo, 18
	v_writelane_b32 v255, s100, 12
	s_add_i32 vcc_lo, vcc_lo, vcc_hi
	v_readlane_b32 vcc_hi, v248, 13
	s_lshl_b32 s100, vcc_lo, 18
	v_writelane_b32 v255, s100, 13
	s_add_i32 vcc_lo, vcc_lo, vcc_hi
	v_readlane_b32 vcc_hi, v248, 14
	s_lshl_b32 s100, vcc_lo, 18
	v_writelane_b32 v255, s100, 14
	s_add_i32 vcc_lo, vcc_lo, vcc_hi
	v_readlane_b32 vcc_hi, v248, 15
	s_lshl_b32 s100, vcc_lo, 18
	v_writelane_b32 v255, s100, 15
	s_add_i32 vcc_lo, vcc_lo, vcc_hi
	v_mov_b32_e32 v92, v0
	v_readlane_b32 s0, v246, 7
	v_ashrrev_i32_e32 v1, 6, v92
	v_readlane_b32 s4, v242, 20
	v_add_u32_e32 v1, s0, v1
	v_readlane_b32 s0, v243, 63
	v_readlane_b32 s5, v242, 21
	s_movk_i32 s6, 0x6000
	v_mul_lo_u32 v84, v1, s0
	s_lshl_b32 s0, s7, 13
	v_ashrrev_i32_e32 v85, 31, v84
	s_add_u32 s0, s4, s0
	v_lshrrev_b32_e32 v1, 20, v85
	s_addc_u32 s1, s5, 0
	v_readlane_b32 s4, v244, 23
	v_add_u32_e32 v1, v84, v1
	v_readlane_b32 s5, v244, 24
	s_waitcnt vmcnt(7)
	v_ashrrev_i32_e32 v2, 12, v1
	s_mov_b32 s9, s5
	v_readlane_b32 s4, v246, 19
	s_add_i32 s8, s7, -1
	v_ashrrev_i32_e32 v3, 31, v2
	v_readlane_b32 s5, v246, 20
	v_lshlrev_b32_e32 v1, 2, v92
	v_lshl_add_u64 v[4:5], s[8:9], 3, v[2:3]
	s_waitcnt vmcnt(6)
	v_mov_b64_e32 v[6:7], s[4:5]
	v_and_b32_e32 v194, 0xfc, v1
	v_mad_u64_u32 v[8:9], s[4:5], v4, s6, v[6:7]
	v_lshlrev_b32_e32 v10, 2, v194
	v_mov_b32_e32 v11, v195
	v_mad_i32_i24 v9, v5, s6, v9
	v_lshl_add_u64 v[4:5], v[8:9], 0, v[10:11]
	s_mov_b64 s[4:5], 0x5000
	s_waitcnt vmcnt(0)
	v_lshl_add_u64 v[18:19], v[4:5], 0, s[4:5]
	s_lshl_b32 s8, s7, 3
	s_mov_b32 s5, s9
	v_writelane_b32 v244, s4, 23
	v_lshl_add_u64 v[2:3], v[2:3], 0, s[8:9]
	v_lshlrev_b64 v[90:91], 11, v[84:85]
	v_writelane_b32 v244, s5, 24
	v_mad_u64_u32 v[6:7], s[4:5], v2, s6, v[6:7]
	v_mad_i32_i24 v7, v3, s6, v7
	v_lshl_add_u64 v[14:15], v[6:7], 0, v[10:11]
	s_mov_b64 s[4:5], 0x1000
	v_lshl_add_u64 v[20:21], v[14:15], 0, s[4:5]
	s_movk_i32 s4, 0x5000
	v_add_co_u32_e32 v22, vcc, s4, v4
	s_movk_i32 s4, 0x1000
	s_nop 0
	v_addc_co_u32_e32 v23, vcc, 0, v5, vcc
	v_add_co_u32_e32 v68, vcc, s4, v14
	v_lshlrev_b32_e32 v70, 1, v194
	s_nop 0
	v_addc_co_u32_e32 v69, vcc, 0, v15, vcc
	global_load_dwordx4 v[56:59], v10, s[0:1]
	global_load_dwordx4 v[44:47], v10, s[0:1] offset:1024
	global_load_dwordx4 v[2:5], v[14:15], off
	global_load_dwordx4 v[6:9], v[14:15], off offset:1024
	global_load_dwordx4 v[52:55], v[20:21], off offset:1024
	global_load_dwordx4 v[40:43], v[20:21], off offset:2048
	global_load_dwordx4 v[36:39], v10, s[0:1] offset:2048
	global_load_dwordx4 v[24:27], v10, s[0:1] offset:3072
	global_load_dwordx4 v[48:51], v[18:19], off offset:2048
	global_load_dwordx4 v[28:31], v[18:19], off offset:3072
	s_nop 0
	global_load_dwordx4 v[10:13], v[14:15], off offset:2048
	s_nop 0
	global_load_dwordx4 v[14:17], v[14:15], off offset:3072
	s_nop 0
	global_load_dwordx4 v[64:67], v[22:23], off
	global_load_dwordx4 v[32:35], v[20:21], off offset:3072
	v_readlane_b32 s0, v246, 25
	v_readlane_b32 s1, v246, 26
	v_mov_b32_e32 v71, v195
	s_nop 0
	v_lshl_add_u64 v[78:79], v[84:85], 4, s[0:1]
	v_readlane_b32 s0, v246, 23
	v_readlane_b32 s1, v246, 24
	global_load_dwordx4 v[60:63], v[18:19], off offset:1024
	global_load_dwordx4 v[20:23], v[78:79], off
	v_lshl_add_u64 v[18:19], s[0:1], 0, v[90:91]
	v_readlane_b32 s0, v246, 21
	v_readlane_b32 s1, v246, 22
	v_lshl_add_u64 v[18:19], v[18:19], 0, v[70:71]
	global_load_dwordx4 v[68:71], v[68:69], off
	s_nop 0
	global_load_dwordx2 v[74:75], v[18:19], off
	global_load_dwordx2 v[80:81], v[18:19], off offset:512
	global_load_dwordx2 v[76:77], v[18:19], off offset:1024
	global_load_dwordx2 v[72:73], v[18:19], off offset:1536
	s_waitcnt vmcnt(0)
	v_readfirstlane_b32 s100, v20
	s_lshr_b32 s101, s100, 16
	s_and_b32 s100, s100, 0xffff
	s_lshl_b32 s100, s100, 10
	s_nop 1
	v_readlane_b32 s101, v255, s101
	s_add_u32 vcc_lo, s58, 0x14b51000
	s_addc_u32 vcc_hi, s59, 0
	s_add_u32 s100, s100, s101
	s_add_u32 vcc_lo, vcc_lo, s100
	s_addc_u32 vcc_hi, vcc_hi, 0
	global_load_dword v127, v194, vcc
	global_load_dword v126, v194, vcc offset:256
	global_load_dword v124, v194, vcc offset:512
	global_load_dword v122, v194, vcc offset:768
	v_readfirstlane_b32 s100, v21
	s_lshr_b32 s101, s100, 16
	s_and_b32 s100, s100, 0xffff
	s_lshl_b32 s100, s100, 10
	s_nop 1
	v_readlane_b32 s101, v255, s101
	s_add_u32 vcc_lo, s58, 0x14b51000
	s_addc_u32 vcc_hi, s59, 0
	s_add_u32 s100, s100, s101
	s_add_u32 vcc_lo, vcc_lo, s100
	s_addc_u32 vcc_hi, vcc_hi, 0
	global_load_dword v128, v194, vcc
	global_load_dword v125, v194, vcc offset:256
	global_load_dword v123, v194, vcc offset:512
	global_load_dword v121, v194, vcc offset:768
	v_readlane_b32 s0, v242, 2
	v_readlane_b32 s1, v242, 3
	s_andn2_b64 vcc, exec, s[0:1]
	s_waitcnt vmcnt(13)
	v_mov_b64_e32 v[18:19], v[20:21]
	v_mov_b64_e32 v[20:21], v[22:23]
	s_cbranch_vccnz .LBB0_175
	global_load_dwordx4 v[18:21], v[78:79], off offset:16

.LBB0_179:
	v_add_u32_e32 v108, 1, v84
	v_cmp_lt_i32_e32 vcc, v108, v1
	v_cmp_ge_i32_e64 s[0:1], v108, v1
	v_mov_b32_e32 v115, v74
	v_mov_b32_e32 v116, v72
	v_mov_b32_e32 v117, v75
	v_mov_b32_e32 v118, v73
	v_mov_b32_e32 v112, v78
	v_mov_b32_e32 v113, v76
	v_mov_b32_e32 v114, v79
	v_mov_b32_e32 v71, v77
	v_mov_b32_e32 v110, v82
	v_mov_b32_e32 v90, v80
	v_mov_b32_e32 v111, v83
	v_mov_b32_e32 v91, v81
	v_mov_b32_e32 v85, v89
	v_mov_b32_e32 v92, v87
	v_mov_b32_e32 v109, v88
	v_mov_b32_e32 v93, v86
	v_mov_b32_e32 v119, v22
	v_mov_b32_e32 v120, v23
	s_and_saveexec_b64 s[8:9], vcc
	s_cbranch_execz .LBB0_178
	v_lshl_add_u64 v[24:25], v[64:65], 0, s[6:7]
	v_add_co_u32_e32 v24, vcc, 0x2b0d1000, v24
	v_add_u32_e32 v84, 2, v84
	s_nop 0
	v_addc_co_u32_e32 v25, vcc, 0, v25, vcc
	global_load_dwordx2 v[92:93], v[24:25], off
	global_load_dwordx2 v[90:91], v[24:25], off offset:512
	global_load_dwordx2 v[70:71], v[24:25], off offset:1024
	global_load_dwordx2 v[68:69], v[24:25], off offset:1536
	v_readfirstlane_b32 s100, v18
	s_lshr_b32 s101, s100, 16
	s_and_b32 s100, s100, 0xffff
	s_lshl_b32 s100, s100, 10
	s_nop 1
	v_readlane_b32 s101, v255, s101
	s_add_u32 vcc_lo, s58, 0x14b51000
	s_addc_u32 vcc_hi, s59, 0
	s_add_u32 s100, s100, s101
	s_add_u32 vcc_lo, vcc_lo, s100
	s_addc_u32 vcc_hi, vcc_hi, 0
	global_load_dword v100, v194, vcc
	global_load_dword v101, v194, vcc offset:256
	global_load_dword v102, v194, vcc offset:512
	global_load_dword v103, v194, vcc offset:768
	v_readfirstlane_b32 s100, v19
	s_lshr_b32 s101, s100, 16
	s_and_b32 s100, s100, 0xffff
	s_lshl_b32 s100, s100, 10
	s_nop 1
	v_readlane_b32 s101, v255, s101
	s_add_u32 vcc_lo, s58, 0x14b51000
	s_addc_u32 vcc_hi, s59, 0
	s_add_u32 s100, s100, s101
	s_add_u32 vcc_lo, vcc_lo, s100
	s_addc_u32 vcc_hi, vcc_hi, 0
	global_load_dword v104, v194, vcc
	global_load_dword v105, v194, vcc offset:256
	global_load_dword v106, v194, vcc offset:512
	global_load_dword v107, v194, vcc offset:768
	v_mov_b64_e32 v[26:27], v[20:21]
	v_cmp_lt_i32_e32 vcc, v84, v1
	v_mov_b64_e32 v[24:25], v[18:19]
	s_and_saveexec_b64 s[10:11], vcc
	s_cbranch_execz .LBB0_177
	v_readlane_b32 s12, v246, 25
	v_ashrrev_i32_e32 v85, 31, v84
	v_readlane_b32 s13, v246, 26
	s_nop 1
	v_lshl_add_u64 v[18:19], v[84:85], 4, s[12:13]
	global_load_dwordx4 v[24:27], v[18:19], off
	s_branch .LBB0_177

.LBB0_1761:
	s_andn2_b64 vcc, exec, s[0:1]
	s_cbranch_vccnz .LBB0_1818
	s_mov_b64 s[0:1], exec
	v_readlane_b32 s4, v242, 30
	v_readlane_b32 s5, v242, 31
	s_and_b64 s[4:5], s[0:1], s[4:5]
	s_mov_b64 exec, s[4:5]
	s_cbranch_execz .LBB0_1788
	v_readlane_b32 s4, v244, 12
	s_waitcnt vmcnt(0)
	v_mov_b32_e32 v1, s4
	ds_read_b32 v2, v1
	v_readlane_b32 s10, v243, 52
	v_readlane_b32 s8, v243, 0
	s_ashr_i32 s9, s18, 3
	s_waitcnt lgkmcnt(0)
	v_readfirstlane_b32 s6, v2
	s_add_i32 s7, s6, 7
	s_ashr_i32 s7, s7, 3
	s_mul_i32 s8, s7, s8
	s_lshr_b32 s11, s10, 2
	s_add_i32 s12, s8, s11
	s_add_i32 s10, s10, s9
	v_lshl_or_b32 v3, s12, 8, v0
	v_lshlrev_b32_e32 v3, 10, v3
	s_lshr_b32 s11, s10, 2
	s_add_i32 s12, s8, s11
	s_add_i32 s10, s10, s9
	v_lshl_or_b32 v4, s12, 8, v0
	v_lshlrev_b32_e32 v4, 10, v4
	s_lshr_b32 s11, s10, 2
	s_add_i32 s12, s8, s11
	s_add_i32 s10, s10, s9
	v_lshl_or_b32 v5, s12, 8, v0
	v_lshlrev_b32_e32 v5, 10, v5
	s_lshr_b32 s11, s10, 2
	s_add_i32 s12, s8, s11
	s_add_i32 s10, s10, s9
	v_lshl_or_b32 v6, s12, 8, v0
	v_lshlrev_b32_e32 v6, 10, v6
	s_lshr_b32 s11, s10, 2
	s_add_i32 s12, s8, s11
	s_add_i32 s10, s10, s9
	v_lshl_or_b32 v7, s12, 8, v0
	v_lshlrev_b32_e32 v7, 10, v7
	s_lshr_b32 s11, s10, 2
	s_add_i32 s12, s8, s11
	s_add_i32 s10, s10, s9
	v_lshl_or_b32 v8, s12, 8, v0
	v_lshlrev_b32_e32 v8, 10, v8
	ds_write2st64_b32 v200, v3, v4 offset1:4
	ds_write2st64_b32 v200, v5, v6 offset0:8 offset1:12
	ds_write2st64_b32 v200, v7, v8 offset0:16 offset1:20

.LBB0_1944:
	v_readlane_b32 s4, v244, 45
	v_readlane_b32 s5, v244, 46
	s_load_dwordx2 s[2:3], s[4:5], 0xd8
	s_waitcnt lgkmcnt(0)
	s_cmp_le_i32 s2, s66
	s_cselect_b64 s[0:1], -1, 0
	s_cmp_lt_i32 s66, s3
	s_cselect_b64 s[2:3], -1, 0
	s_and_b64 s[0:1], s[0:1], s[2:3]
	s_and_b64 vcc, exec, s[0:1]
	s_cbranch_vccz .LBB0_2008
	v_readlane_b32 s0, v246, 7
	v_ashrrev_i32_e32 v1, 6, v0
	s_waitcnt vmcnt(7)
	v_and_b32_e32 v247, 63, v0
	v_min_u32_e32 v247, 15, v247
	v_lshlrev_b32_e32 v247, 8, v247
	v_add_u32_e32 v247, 0x7000, v247
	v_readlane_b32 s100, v244, 55
	v_readlane_b32 s101, v244, 56
	s_nop 4
	global_load_dword v248, v247, s[100:101] sc1
	s_waitcnt vmcnt(0)
	v_add_u32_e32 v248, 0xff, v248
	v_lshrrev_b32_e32 v248, 8, v248
	s_mov_b32 vcc_lo, 0
	v_readlane_b32 vcc_hi, v248, 0
	s_lshl_b32 s100, vcc_lo, 18
	v_writelane_b32 v255, s100, 0
	s_add_i32 vcc_lo, vcc_lo, vcc_hi
	v_readlane_b32 vcc_hi, v248, 1
	s_lshl_b32 s100, vcc_lo, 18
	v_writelane_b32 v255, s100, 1
	s_add_i32 vcc_lo, vcc_lo, vcc_hi
	v_readlane_b32 vcc_hi, v248, 2
	s_lshl_b32 s100, vcc_lo, 18
	v_writelane_b32 v255, s100, 2
	s_add_i32 vcc_lo, vcc_lo, vcc_hi
	v_readlane_b32 vcc_hi, v248, 3
	s_lshl_b32 s100, vcc_lo, 18
	v_writelane_b32 v255, s100, 3
	s_add_i32 vcc_lo, vcc_lo, vcc_hi
	v_readlane_b32 vcc_hi, v248, 4
	s_lshl_b32 s100, vcc_lo, 18
	v_writelane_b32 v255, s100, 4
	s_add_i32 vcc_lo, vcc_lo, vcc_hi
	v_readlane_b32 vcc_hi, v248, 5
	s_lshl_b32 s100, vcc_lo, 18
	v_writelane_b32 v255, s100, 5
	s_add_i32 vcc_lo, vcc_lo, vcc_hi
	v_readlane_b32 vcc_hi, v248, 6
	s_lshl_b32 s100, vcc_lo, 18
	v_writelane_b32 v255, s100, 6
	s_add_i32 vcc_lo, vcc_lo, vcc_hi
	v_readlane_b32 vcc_hi, v248, 7
	s_lshl_b32 s100, vcc_lo, 18
	v_writelane_b32 v255, s100, 7
	s_add_i32 vcc_lo, vcc_lo, vcc_hi
	v_readlane_b32 vcc_hi, v248, 8
	s_lshl_b32 s100, vcc_lo, 18
	v_writelane_b32 v255, s100, 8
	s_add_i32 vcc_lo, vcc_lo, vcc_hi
	v_readlane_b32 vcc_hi, v248, 9
	s_lshl_b32 s100, vcc_lo, 18
	v_writelane_b32 v255, s100, 9
	s_add_i32 vcc_lo, vcc_lo, vcc_hi
	v_readlane_b32 vcc_hi, v248, 10
	s_lshl_b32 s100, vcc_lo, 18
	v_writelane_b32 v255, s100, 10
	s_add_i32 vcc_lo, vcc_lo, vcc_hi
	v_readlane_b32 vcc_hi, v248, 11
	s_lshl_b32 s100, vcc_lo, 18
	v_writelane_b32 v255, s100, 11
	s_add_i32 vcc_lo, vcc_lo, vcc_hi
	v_readlane_b32 vcc_hi, v248, 12
	s_lshl_b32 s100, vcc_lo, 18
	v_writelane_b32 v255, s100, 12
	s_add_i32 vcc_lo, vcc_lo, vcc_hi
	v_readlane_b32 vcc_hi, v248, 13
	s_lshl_b32 s100, vcc_lo, 18
	v_writelane_b32 v255, s100, 13
	s_add_i32 vcc_lo, vcc_lo, vcc_hi
	v_readlane_b32 vcc_hi, v248, 14
	s_lshl_b32 s100, vcc_lo, 18
	v_writelane_b32 v255, s100, 14
	s_add_i32 vcc_lo, vcc_lo, vcc_hi
	v_readlane_b32 vcc_hi, v248, 15
	s_lshl_b32 s100, vcc_lo, 18
	v_writelane_b32 v255, s100, 15
	s_add_i32 vcc_lo, vcc_lo, vcc_hi
	v_lshlrev_b32_e32 v2, 2, v0
	v_add_u32_e32 v1, s0, v1
	v_readlane_b32 s0, v243, 63
	s_waitcnt vmcnt(6)
	v_and_b32_e32 v40, 0xfc, v2
	v_mov_b32_e32 v41, 0
	s_waitcnt vmcnt(5)
	v_mul_lo_u32 v48, v1, s0
	v_ashrrev_i32_e32 v49, 31, v48
	v_lshrrev_b32_e32 v1, 20, v49
	v_add_u32_e32 v1, v48, v1
	v_ashrrev_i32_e32 v1, 12, v1
	v_mul_i32_i24_e32 v2, 6, v1
	v_ashrrev_i32_e32 v3, 31, v2
	s_load_dwordx2 s[0:1], s[4:5], 0x28
	v_lshlrev_b64 v[2:3], 12, v[2:3]
	v_lshlrev_b32_e32 v14, 2, v40
	v_mov_b32_e32 v15, v41
	v_lshl_add_u64 v[2:3], s[58:59], 0, v[2:3]
	v_lshl_add_u64 v[2:3], v[2:3], 0, v[14:15]
	s_mov_b64 s[2:3], 0xa5000
	s_waitcnt vmcnt(0)
	v_lshl_add_u64 v[18:19], v[2:3], 0, s[2:3]
	s_mov_b32 s2, 0xa5000
	v_add_co_u32_e32 v20, vcc, s2, v2
	v_lshlrev_b32_e32 v42, 1, v40
	s_nop 0
	v_addc_co_u32_e32 v21, vcc, 0, v3, vcc
	s_waitcnt lgkmcnt(0)
	global_load_dwordx4 v[2:5], v14, s[0:1]
	global_load_dwordx4 v[6:9], v14, s[0:1] offset:1024
	global_load_dwordx4 v[32:35], v[18:19], off offset:1024
	global_load_dwordx4 v[24:27], v[18:19], off offset:2048
	global_load_dwordx4 v[10:13], v14, s[0:1] offset:2048
	s_nop 0
	global_load_dwordx4 v[14:17], v14, s[0:1] offset:3072
	s_nop 0
	global_load_dwordx4 v[36:39], v[20:21], off
	global_load_dwordx4 v[28:31], v[18:19], off offset:3072
	v_lshlrev_b64 v[18:19], 11, v[48:49]
	v_mov_b32_e32 v43, v41
	v_lshl_add_u64 v[18:19], s[58:59], 0, v[18:19]
	v_lshl_add_u64 v[42:43], v[18:19], 0, v[42:43]
	s_mov_b64 s[2:3], 0x2b0d1000
	s_add_u32 s0, s58, 0xd1000
	v_lshl_add_u64 v[54:55], v[42:43], 0, s[2:3]
	s_mov_b32 s2, 0x2b0d1000
	s_addc_u32 s1, s59, 0
	v_add_co_u32_e32 v42, vcc, s2, v42
	v_lshl_add_u64 v[50:51], v[48:49], 4, s[0:1]
	s_nop 0
	v_addc_co_u32_e32 v43, vcc, 0, v43, vcc
	v_lshl_add_u64 v[18:19], v[18:19], 0, v[40:41]
	s_mov_b64 s[2:3], 0x14b51000
	global_load_dwordx4 v[20:23], v[50:51], off
	global_load_dwordx2 v[52:53], v[42:43], off
	global_load_dwordx2 v[46:47], v[54:55], off offset:512
	global_load_dwordx2 v[44:45], v[54:55], off offset:1024
	s_nop 0
	global_load_dwordx2 v[42:43], v[54:55], off offset:1536
	s_waitcnt vmcnt(0)
	v_readfirstlane_b32 s100, v20
	s_lshr_b32 s101, s100, 16
	s_and_b32 s100, s100, 0xffff
	s_lshl_b32 s100, s100, 10
	s_nop 1
	v_readlane_b32 s101, v255, s101
	s_add_u32 vcc_lo, s58, 0x14b51000
	s_addc_u32 vcc_hi, s59, 0
	s_add_u32 s100, s100, s101
	s_add_u32 vcc_lo, vcc_lo, s100
	s_addc_u32 vcc_hi, vcc_hi, 0
	global_load_dword v98, v40, vcc
	global_load_dword v89, v40, vcc offset:256
	global_load_dword v87, v40, vcc offset:512
	global_load_dword v85, v40, vcc offset:768
	v_readfirstlane_b32 s100, v21
	s_lshr_b32 s101, s100, 16
	s_and_b32 s100, s100, 0xffff
	s_lshl_b32 s100, s100, 10
	s_nop 1
	v_readlane_b32 s101, v255, s101
	s_add_u32 vcc_lo, s58, 0x14b51000
	s_addc_u32 vcc_hi, s59, 0
	s_add_u32 s100, s100, s101
	s_add_u32 vcc_lo, vcc_lo, s100
	s_addc_u32 vcc_hi, vcc_hi, 0
	global_load_dword v99, v40, vcc
	global_load_dword v92, v40, vcc offset:256
	global_load_dword v88, v40, vcc offset:512
	global_load_dword v86, v40, vcc offset:768
	v_cmp_ne_u32_e32 vcc, 1, v197
	s_waitcnt vmcnt(12)
	v_mov_b64_e32 v[18:19], v[20:21]
	v_mov_b64_e32 v[20:21], v[22:23]
	s_cbranch_vccnz .LBB0_1947
	global_load_dwordx4 v[18:21], v[50:51], off offset:16

.LBB0_1951:
	v_add_u32_e32 v100, -1, v46
	v_cmp_lt_i32_e32 vcc, v100, v69
	v_mov_b32_e32 v108, v68
	v_mov_b32_e32 v109, v22
	v_mov_b32_e32 v106, v54
	v_mov_b32_e32 v70, v55
	v_mov_b32_e32 v107, v52
	v_mov_b32_e32 v71, v53
	v_mov_b32_e32 v104, v58
	v_mov_b32_e32 v72, v59
	v_mov_b32_e32 v105, v56
	v_mov_b32_e32 v73, v57
	v_mov_b32_e32 v102, v62
	v_mov_b32_e32 v74, v63
	v_mov_b32_e32 v103, v60
	v_mov_b32_e32 v75, v61
	v_mov_b32_e32 v47, v66
	v_mov_b32_e32 v76, v67
	v_mov_b32_e32 v101, v64
	v_mov_b32_e32 v77, v65
	s_and_saveexec_b64 s[8:9], vcc
	s_cbranch_execz .LBB0_1950
	v_lshl_add_u64 v[24:25], v[48:49], 0, v[50:51]
	v_add_co_u32_e32 v24, vcc, 0x2b0d1000, v24
	s_nop 1
	v_addc_co_u32_e32 v25, vcc, 0, v25, vcc
	global_load_dwordx2 v[76:77], v[24:25], off
	global_load_dwordx2 v[74:75], v[24:25], off offset:512
	global_load_dwordx2 v[72:73], v[24:25], off offset:1024
	global_load_dwordx2 v[70:71], v[24:25], off offset:1536
	v_readfirstlane_b32 s100, v18
	s_lshr_b32 s101, s100, 16
	s_and_b32 s100, s100, 0xffff
	s_lshl_b32 s100, s100, 10
	s_nop 1
	v_readlane_b32 s101, v255, s101
	s_add_u32 vcc_lo, s58, 0x14b51000
	s_addc_u32 vcc_hi, s59, 0
	s_add_u32 s100, s100, s101
	s_add_u32 vcc_lo, vcc_lo, s100
	s_addc_u32 vcc_hi, vcc_hi, 0
	global_load_dword v23, v40, vcc
	global_load_dword v90, v40, vcc offset:256
	global_load_dword v91, v40, vcc offset:512
	global_load_dword v93, v40, vcc offset:768
	v_readfirstlane_b32 s100, v19
	s_lshr_b32 s101, s100, 16
	s_and_b32 s100, s100, 0xffff
	s_lshl_b32 s100, s100, 10
	s_nop 1
	v_readlane_b32 s101, v255, s101
	s_add_u32 vcc_lo, s58, 0x14b51000
	s_addc_u32 vcc_hi, s59, 0
	s_add_u32 s100, s100, s101
	s_add_u32 vcc_lo, vcc_lo, s100
	s_addc_u32 vcc_hi, vcc_hi, 0
	global_load_dword v94, v40, vcc
	global_load_dword v95, v40, vcc offset:256
	global_load_dword v96, v40, vcc offset:512
	global_load_dword v97, v40, vcc offset:768
	v_mov_b64_e32 v[26:27], v[20:21]
	v_cmp_lt_i32_e32 vcc, v46, v69
	v_mov_b64_e32 v[24:25], v[18:19]
	s_and_saveexec_b64 s[10:11], vcc
	s_cbranch_execz .LBB0_1949
	v_ashrrev_i32_e32 v47, 31, v46
	v_lshl_add_u64 v[18:19], v[46:47], 4, s[0:1]
	global_load_dwordx4 v[24:27], v[18:19], off
	s_branch .LBB0_1949
